# un-aligned half epilogues in w1 and G_in GEMMs: leading half skips the K-loop-exit barrier when another unit follows, trailing half skips the re-stagger barrier (on v16)
# baseline (speedup 1.0000x reference)
.Lrx_hgrn1_w2:
	s_waitcnt vmcnt(24)
	s_mov_b32 s32, 0
	s_waitcnt lgkmcnt(0)
	s_barrier
	s_setprio 1
	s_waitcnt lgkmcnt(0)
	v_mfma_f32_16x16x32_bf16 v[128:131], v[132:135], v[202:205], v[128:131]
	v_mfma_f32_16x16x32_bf16 v[124:127], v[152:155], v[202:205], v[124:127]
	v_mfma_f32_16x16x32_bf16 v[110:113], v[132:135], v[210:213], v[110:113]
	v_mfma_f32_16x16x32_bf16 v[106:109], v[152:155], v[210:213], v[106:109]
	v_mfma_f32_16x16x32_bf16 v[94:97], v[132:135], v[218:221], v[94:97]
	v_mfma_f32_16x16x32_bf16 v[90:93], v[152:155], v[218:221], v[90:93]
	v_mfma_f32_16x16x32_bf16 v[78:81], v[132:135], v[226:229], v[78:81]
	v_mfma_f32_16x16x32_bf16 v[74:77], v[152:155], v[226:229], v[74:77]
	v_mfma_f32_16x16x32_bf16 v[128:131], v[136:139], v[206:209], v[128:131]
	v_mfma_f32_16x16x32_bf16 v[124:127], v[166:169], v[206:209], v[124:127]
	v_mfma_f32_16x16x32_bf16 v[110:113], v[136:139], v[214:217], v[110:113]
	v_mfma_f32_16x16x32_bf16 v[106:109], v[166:169], v[214:217], v[106:109]
	v_mfma_f32_16x16x32_bf16 v[94:97], v[136:139], v[222:225], v[94:97]
	v_mfma_f32_16x16x32_bf16 v[90:93], v[166:169], v[222:225], v[90:93]
	v_mfma_f32_16x16x32_bf16 v[78:81], v[136:139], v[230:233], v[78:81]
	v_mfma_f32_16x16x32_bf16 v[74:77], v[166:169], v[230:233], v[74:77]
	s_setprio 0
	s_setprio 1
	v_mfma_f32_16x16x32_bf16 v[120:123], v[176:179], v[202:205], v[120:123]
	v_mfma_f32_16x16x32_bf16 v[116:119], v[194:197], v[202:205], v[116:119]
	v_mfma_f32_16x16x32_bf16 v[102:105], v[176:179], v[210:213], v[102:105]
	v_mfma_f32_16x16x32_bf16 v[98:101], v[194:197], v[210:213], v[98:101]
	v_mfma_f32_16x16x32_bf16 v[86:89], v[176:179], v[218:221], v[86:89]
	v_mfma_f32_16x16x32_bf16 v[82:85], v[194:197], v[218:221], v[82:85]
	v_mfma_f32_16x16x32_bf16 v[70:73], v[176:179], v[226:229], v[70:73]
	v_mfma_f32_16x16x32_bf16 v[66:69], v[194:197], v[226:229], v[66:69]
	v_mfma_f32_16x16x32_bf16 v[120:123], v[180:183], v[206:209], v[120:123]
	v_mfma_f32_16x16x32_bf16 v[116:119], v[198:201], v[206:209], v[116:119]
	v_mfma_f32_16x16x32_bf16 v[102:105], v[180:183], v[214:217], v[102:105]
	v_mfma_f32_16x16x32_bf16 v[98:101], v[198:201], v[214:217], v[98:101]
	v_mfma_f32_16x16x32_bf16 v[86:89], v[180:183], v[222:225], v[86:89]
	v_mfma_f32_16x16x32_bf16 v[82:85], v[198:201], v[222:225], v[82:85]
	v_mfma_f32_16x16x32_bf16 v[70:73], v[180:183], v[230:233], v[70:73]
	v_mfma_f32_16x16x32_bf16 v[66:69], v[198:201], v[230:233], v[66:69]
	s_setprio 0
	s_barrier
	s_add_u32 s62, s60, 0x8000
	s_addc_u32 s63, s61, 0
	s_add_i32 s16, s16, s4
	s_mov_b32 m0, s16
	ds_read_b128 v[202:205], v175 offset:49152
	ds_read_b128 v[206:209], v175 offset:50176
	ds_read_b128 v[210:213], v175 offset:51200
	ds_read_b128 v[214:217], v175 offset:52224
	ds_read_b128 v[218:221], v175 offset:53248
	ds_read_b128 v[222:225], v175 offset:54272
	ds_read_b128 v[226:229], v175 offset:55296
	ds_read_b128 v[230:233], v175 offset:56320
	global_load_lds_dwordx4 v142, s[62:63]
	s_add_i32 m0, s16, 0x2000
	s_add_u32 s60, s60, 0x9000
	s_addc_u32 s61, s61, 0
	s_add_i32 s16, s17, s4
	global_load_lds_dwordx4 v146, s[62:63]
	s_mov_b32 m0, s16
	s_nop 0
	global_load_lds_dwordx4 v142, s[60:61]
	s_add_i32 m0, s16, 0x2000
	s_nop 0
	global_load_lds_dwordx4 v146, s[60:61]
	s_mov_b32 m0, s65
	s_nop 0
	global_load_lds_dwordx4 v140, s[58:59]
	s_mov_b32 m0, s66
	s_nop 0
	global_load_lds_dwordx4 v144, s[58:59]
	s_waitcnt vmcnt(8)
	s_waitcnt lgkmcnt(0)
	s_barrier
	s_setprio 1
	s_waitcnt lgkmcnt(0)
	v_mfma_f32_16x16x32_bf16 v[62:65], v[132:135], v[202:205], v[62:65]
	v_mfma_f32_16x16x32_bf16 v[58:61], v[152:155], v[202:205], v[58:61]
	v_mfma_f32_16x16x32_bf16 v[46:49], v[132:135], v[210:213], v[46:49]
	v_mfma_f32_16x16x32_bf16 v[42:45], v[152:155], v[210:213], v[42:45]
	v_mfma_f32_16x16x32_bf16 v[30:33], v[132:135], v[218:221], v[30:33]
	v_mfma_f32_16x16x32_bf16 v[26:29], v[152:155], v[218:221], v[26:29]
	v_mfma_f32_16x16x32_bf16 v[14:17], v[132:135], v[226:229], v[14:17]
	v_mfma_f32_16x16x32_bf16 v[10:13], v[152:155], v[226:229], v[10:13]
	v_mfma_f32_16x16x32_bf16 v[62:65], v[136:139], v[206:209], v[62:65]
	v_mfma_f32_16x16x32_bf16 v[58:61], v[166:169], v[206:209], v[58:61]
	v_mfma_f32_16x16x32_bf16 v[46:49], v[136:139], v[214:217], v[46:49]
	v_mfma_f32_16x16x32_bf16 v[42:45], v[166:169], v[214:217], v[42:45]
	v_mfma_f32_16x16x32_bf16 v[30:33], v[136:139], v[222:225], v[30:33]
	v_mfma_f32_16x16x32_bf16 v[26:29], v[166:169], v[222:225], v[26:29]
	v_mfma_f32_16x16x32_bf16 v[14:17], v[136:139], v[230:233], v[14:17]
	v_mfma_f32_16x16x32_bf16 v[10:13], v[166:169], v[230:233], v[10:13]
	s_setprio 0
	s_setprio 1
	v_mfma_f32_16x16x32_bf16 v[54:57], v[176:179], v[202:205], v[54:57]
	v_mfma_f32_16x16x32_bf16 v[50:53], v[194:197], v[202:205], v[50:53]
	v_mfma_f32_16x16x32_bf16 v[38:41], v[176:179], v[210:213], v[38:41]
	v_mfma_f32_16x16x32_bf16 v[34:37], v[194:197], v[210:213], v[34:37]
	v_mfma_f32_16x16x32_bf16 v[22:25], v[176:179], v[218:221], v[22:25]
	v_mfma_f32_16x16x32_bf16 v[18:21], v[194:197], v[218:221], v[18:21]
	v_mfma_f32_16x16x32_bf16 v[6:9], v[176:179], v[226:229], v[6:9]
	v_mfma_f32_16x16x32_bf16 v[2:5], v[194:197], v[226:229], v[2:5]
	v_mfma_f32_16x16x32_bf16 v[54:57], v[180:183], v[206:209], v[54:57]
	v_mfma_f32_16x16x32_bf16 v[50:53], v[198:201], v[206:209], v[50:53]
	v_mfma_f32_16x16x32_bf16 v[38:41], v[180:183], v[214:217], v[38:41]
	v_mfma_f32_16x16x32_bf16 v[34:37], v[198:201], v[214:217], v[34:37]
	v_mfma_f32_16x16x32_bf16 v[22:25], v[180:183], v[222:225], v[22:25]
	v_mfma_f32_16x16x32_bf16 v[18:21], v[198:201], v[222:225], v[18:21]
	v_mfma_f32_16x16x32_bf16 v[6:9], v[180:183], v[230:233], v[6:9]
	v_mfma_f32_16x16x32_bf16 v[2:5], v[198:201], v[230:233], v[2:5]
	s_setprio 0
	s_barrier
	s_add_i32 s70, s70, 2
	s_add_u32 s56, s56, 0x10000
	s_addc_u32 s57, s57, 0
	s_add_u32 s51, s51, 0x10000
	s_addc_u32 s69, s69, 0
	s_cmp_gt_u32 s70, 29
	s_cbranch_scc0 .LBB0_346
	s_add_u32 s100, s29, 0xc000
	s_addc_u32 s101, s15, 0
	v_lshl_add_u64 v[158:159], s[100:101], 0, v[148:149]
	s_add_i32 m0, s13, 0xc000
	s_nop 0
	global_load_lds_dwordx4 v[158:159], off
	v_lshl_add_u64 v[158:159], s[100:101], 0, v[150:151]
	s_add_i32 m0, s13, 0xe000
	s_nop 0
	global_load_lds_dwordx4 v[158:159], off
	s_andn2_b64 vcc, s[46:47], s[38:39]
	s_cbranch_vccz .LBB0_349
	s_barrier

.LBB0_386:
	s_andn2_b64 vcc, exec, s[0:1]
	s_cbranch_vccnz .LBB0_337
	s_branch .LBB0_337

.Lrx_hgrn2_w2:
	s_waitcnt vmcnt(24)
	s_mov_b32 s32, 0
	s_waitcnt lgkmcnt(0)
	s_barrier
	s_setprio 1
	s_waitcnt lgkmcnt(0)
	v_mfma_f32_16x16x32_bf16 v[128:131], v[132:135], v[202:205], v[128:131]
	v_mfma_f32_16x16x32_bf16 v[124:127], v[152:155], v[202:205], v[124:127]
	v_mfma_f32_16x16x32_bf16 v[110:113], v[132:135], v[210:213], v[110:113]
	v_mfma_f32_16x16x32_bf16 v[106:109], v[152:155], v[210:213], v[106:109]
	v_mfma_f32_16x16x32_bf16 v[94:97], v[132:135], v[218:221], v[94:97]
	v_mfma_f32_16x16x32_bf16 v[90:93], v[152:155], v[218:221], v[90:93]
	v_mfma_f32_16x16x32_bf16 v[78:81], v[132:135], v[226:229], v[78:81]
	v_mfma_f32_16x16x32_bf16 v[74:77], v[152:155], v[226:229], v[74:77]
	v_mfma_f32_16x16x32_bf16 v[128:131], v[136:139], v[206:209], v[128:131]
	v_mfma_f32_16x16x32_bf16 v[124:127], v[166:169], v[206:209], v[124:127]
	v_mfma_f32_16x16x32_bf16 v[110:113], v[136:139], v[214:217], v[110:113]
	v_mfma_f32_16x16x32_bf16 v[106:109], v[166:169], v[214:217], v[106:109]
	v_mfma_f32_16x16x32_bf16 v[94:97], v[136:139], v[222:225], v[94:97]
	v_mfma_f32_16x16x32_bf16 v[90:93], v[166:169], v[222:225], v[90:93]
	v_mfma_f32_16x16x32_bf16 v[78:81], v[136:139], v[230:233], v[78:81]
	v_mfma_f32_16x16x32_bf16 v[74:77], v[166:169], v[230:233], v[74:77]
	s_setprio 0
	s_setprio 1
	v_mfma_f32_16x16x32_bf16 v[120:123], v[176:179], v[202:205], v[120:123]
	v_mfma_f32_16x16x32_bf16 v[116:119], v[194:197], v[202:205], v[116:119]
	v_mfma_f32_16x16x32_bf16 v[102:105], v[176:179], v[210:213], v[102:105]
	v_mfma_f32_16x16x32_bf16 v[98:101], v[194:197], v[210:213], v[98:101]
	v_mfma_f32_16x16x32_bf16 v[86:89], v[176:179], v[218:221], v[86:89]
	v_mfma_f32_16x16x32_bf16 v[82:85], v[194:197], v[218:221], v[82:85]
	v_mfma_f32_16x16x32_bf16 v[70:73], v[176:179], v[226:229], v[70:73]
	v_mfma_f32_16x16x32_bf16 v[66:69], v[194:197], v[226:229], v[66:69]
	v_mfma_f32_16x16x32_bf16 v[120:123], v[180:183], v[206:209], v[120:123]
	v_mfma_f32_16x16x32_bf16 v[116:119], v[198:201], v[206:209], v[116:119]
	v_mfma_f32_16x16x32_bf16 v[102:105], v[180:183], v[214:217], v[102:105]
	v_mfma_f32_16x16x32_bf16 v[98:101], v[198:201], v[214:217], v[98:101]
	v_mfma_f32_16x16x32_bf16 v[86:89], v[180:183], v[222:225], v[86:89]
	v_mfma_f32_16x16x32_bf16 v[82:85], v[198:201], v[222:225], v[82:85]
	v_mfma_f32_16x16x32_bf16 v[70:73], v[180:183], v[230:233], v[70:73]
	v_mfma_f32_16x16x32_bf16 v[66:69], v[198:201], v[230:233], v[66:69]
	s_setprio 0
	s_barrier
	s_add_u32 s60, s58, 0x8000
	s_addc_u32 s61, s59, 0
	s_add_i32 s16, s16, s4
	s_mov_b32 m0, s16
	ds_read_b128 v[202:205], v175 offset:49152
	ds_read_b128 v[206:209], v175 offset:50176
	ds_read_b128 v[210:213], v175 offset:51200
	ds_read_b128 v[214:217], v175 offset:52224
	ds_read_b128 v[218:221], v175 offset:53248
	ds_read_b128 v[222:225], v175 offset:54272
	ds_read_b128 v[226:229], v175 offset:55296
	ds_read_b128 v[230:233], v175 offset:56320
	global_load_lds_dwordx4 v142, s[60:61]
	s_add_i32 m0, s16, 0x2000
	s_add_u32 s58, s58, 0x9000
	s_addc_u32 s59, s59, 0
	s_add_i32 s16, s17, s4
	global_load_lds_dwordx4 v146, s[60:61]
	s_mov_b32 m0, s16
	s_nop 0
	global_load_lds_dwordx4 v142, s[58:59]
	s_add_i32 m0, s16, 0x2000
	s_nop 0
	global_load_lds_dwordx4 v146, s[58:59]
	s_mov_b32 m0, s62
	s_nop 0
	global_load_lds_dwordx4 v140, s[56:57]
	s_mov_b32 m0, s63
	s_nop 0
	global_load_lds_dwordx4 v144, s[56:57]
	s_waitcnt vmcnt(8)
	s_waitcnt lgkmcnt(0)
	s_barrier
	s_setprio 1
	s_waitcnt lgkmcnt(0)
	v_mfma_f32_16x16x32_bf16 v[62:65], v[132:135], v[202:205], v[62:65]
	v_mfma_f32_16x16x32_bf16 v[58:61], v[152:155], v[202:205], v[58:61]
	v_mfma_f32_16x16x32_bf16 v[46:49], v[132:135], v[210:213], v[46:49]
	v_mfma_f32_16x16x32_bf16 v[42:45], v[152:155], v[210:213], v[42:45]
	v_mfma_f32_16x16x32_bf16 v[30:33], v[132:135], v[218:221], v[30:33]
	v_mfma_f32_16x16x32_bf16 v[26:29], v[152:155], v[218:221], v[26:29]
	v_mfma_f32_16x16x32_bf16 v[14:17], v[132:135], v[226:229], v[14:17]
	v_mfma_f32_16x16x32_bf16 v[10:13], v[152:155], v[226:229], v[10:13]
	v_mfma_f32_16x16x32_bf16 v[62:65], v[136:139], v[206:209], v[62:65]
	v_mfma_f32_16x16x32_bf16 v[58:61], v[166:169], v[206:209], v[58:61]
	v_mfma_f32_16x16x32_bf16 v[46:49], v[136:139], v[214:217], v[46:49]
	v_mfma_f32_16x16x32_bf16 v[42:45], v[166:169], v[214:217], v[42:45]
	v_mfma_f32_16x16x32_bf16 v[30:33], v[136:139], v[222:225], v[30:33]
	v_mfma_f32_16x16x32_bf16 v[26:29], v[166:169], v[222:225], v[26:29]
	v_mfma_f32_16x16x32_bf16 v[14:17], v[136:139], v[230:233], v[14:17]
	v_mfma_f32_16x16x32_bf16 v[10:13], v[166:169], v[230:233], v[10:13]
	s_setprio 0
	s_setprio 1
	v_mfma_f32_16x16x32_bf16 v[54:57], v[176:179], v[202:205], v[54:57]
	v_mfma_f32_16x16x32_bf16 v[50:53], v[194:197], v[202:205], v[50:53]
	v_mfma_f32_16x16x32_bf16 v[38:41], v[176:179], v[210:213], v[38:41]
	v_mfma_f32_16x16x32_bf16 v[34:37], v[194:197], v[210:213], v[34:37]
	v_mfma_f32_16x16x32_bf16 v[22:25], v[176:179], v[218:221], v[22:25]
	v_mfma_f32_16x16x32_bf16 v[18:21], v[194:197], v[218:221], v[18:21]
	v_mfma_f32_16x16x32_bf16 v[6:9], v[176:179], v[226:229], v[6:9]
	v_mfma_f32_16x16x32_bf16 v[2:5], v[194:197], v[226:229], v[2:5]
	v_mfma_f32_16x16x32_bf16 v[54:57], v[180:183], v[206:209], v[54:57]
	v_mfma_f32_16x16x32_bf16 v[50:53], v[198:201], v[206:209], v[50:53]
	v_mfma_f32_16x16x32_bf16 v[38:41], v[180:183], v[214:217], v[38:41]
	v_mfma_f32_16x16x32_bf16 v[34:37], v[198:201], v[214:217], v[34:37]
	v_mfma_f32_16x16x32_bf16 v[22:25], v[180:183], v[222:225], v[22:25]
	v_mfma_f32_16x16x32_bf16 v[18:21], v[198:201], v[222:225], v[18:21]
	v_mfma_f32_16x16x32_bf16 v[6:9], v[180:183], v[230:233], v[6:9]
	v_mfma_f32_16x16x32_bf16 v[2:5], v[198:201], v[230:233], v[2:5]
	s_setprio 0
	s_barrier
	s_add_i32 s67, s67, 2
	s_add_u32 s54, s54, 0x10000
	s_addc_u32 s55, s55, 0
	s_add_u32 s49, s49, 0x10000
	s_addc_u32 s66, s66, 0
	s_cmp_gt_u32 s67, 29
	s_cbranch_scc0 .LBB0_503
	s_add_u32 s100, s29, 0xc000
	s_addc_u32 s101, s15, 0
	v_lshl_add_u64 v[158:159], s[100:101], 0, v[148:149]
	s_add_i32 m0, s12, 0xc000
	s_nop 0
	global_load_lds_dwordx4 v[158:159], off
	v_lshl_add_u64 v[158:159], s[100:101], 0, v[150:151]
	s_add_i32 m0, s12, 0xe000
	s_nop 0
	global_load_lds_dwordx4 v[158:159], off
	s_andn2_b64 vcc, s[44:45], s[38:39]
	s_cbranch_vccz .LBB0_506
	s_barrier

.Lrx_relu2_w2:
	s_waitcnt vmcnt(24)
	s_mov_b32 s32, 0
	s_waitcnt lgkmcnt(0)
	s_barrier
	s_setprio 1
	s_waitcnt lgkmcnt(0)
	v_mfma_f32_16x16x32_bf16 v[128:131], v[148:151], v[198:201], v[128:131]
	v_mfma_f32_16x16x32_bf16 v[124:127], v[158:161], v[198:201], v[124:127]
	v_mfma_f32_16x16x32_bf16 v[110:113], v[148:151], v[206:209], v[110:113]
	v_mfma_f32_16x16x32_bf16 v[106:109], v[158:161], v[206:209], v[106:109]
	v_mfma_f32_16x16x32_bf16 v[94:97], v[148:151], v[214:217], v[94:97]
	v_mfma_f32_16x16x32_bf16 v[90:93], v[158:161], v[214:217], v[90:93]
	v_mfma_f32_16x16x32_bf16 v[78:81], v[148:151], v[222:225], v[78:81]
	v_mfma_f32_16x16x32_bf16 v[74:77], v[158:161], v[222:225], v[74:77]
	v_mfma_f32_16x16x32_bf16 v[128:131], v[152:155], v[202:205], v[128:131]
	v_mfma_f32_16x16x32_bf16 v[124:127], v[166:169], v[202:205], v[124:127]
	v_mfma_f32_16x16x32_bf16 v[110:113], v[152:155], v[210:213], v[110:113]
	v_mfma_f32_16x16x32_bf16 v[106:109], v[166:169], v[210:213], v[106:109]
	v_mfma_f32_16x16x32_bf16 v[94:97], v[152:155], v[218:221], v[94:97]
	v_mfma_f32_16x16x32_bf16 v[90:93], v[166:169], v[218:221], v[90:93]
	v_mfma_f32_16x16x32_bf16 v[78:81], v[152:155], v[226:229], v[78:81]
	v_mfma_f32_16x16x32_bf16 v[74:77], v[166:169], v[226:229], v[74:77]
	s_setprio 0
	s_setprio 1
	v_mfma_f32_16x16x32_bf16 v[120:123], v[170:173], v[198:201], v[120:123]
	v_mfma_f32_16x16x32_bf16 v[116:119], v[178:181], v[198:201], v[116:119]
	v_mfma_f32_16x16x32_bf16 v[102:105], v[170:173], v[206:209], v[102:105]
	v_mfma_f32_16x16x32_bf16 v[98:101], v[178:181], v[206:209], v[98:101]
	v_mfma_f32_16x16x32_bf16 v[86:89], v[170:173], v[214:217], v[86:89]
	v_mfma_f32_16x16x32_bf16 v[82:85], v[178:181], v[214:217], v[82:85]
	v_mfma_f32_16x16x32_bf16 v[70:73], v[170:173], v[222:225], v[70:73]
	v_mfma_f32_16x16x32_bf16 v[66:69], v[178:181], v[222:225], v[66:69]
	v_mfma_f32_16x16x32_bf16 v[120:123], v[174:177], v[202:205], v[120:123]
	v_mfma_f32_16x16x32_bf16 v[116:119], v[194:197], v[202:205], v[116:119]
	v_mfma_f32_16x16x32_bf16 v[102:105], v[174:177], v[210:213], v[102:105]
	v_mfma_f32_16x16x32_bf16 v[98:101], v[194:197], v[210:213], v[98:101]
	v_mfma_f32_16x16x32_bf16 v[86:89], v[174:177], v[218:221], v[86:89]
	v_mfma_f32_16x16x32_bf16 v[82:85], v[194:197], v[218:221], v[82:85]
	v_mfma_f32_16x16x32_bf16 v[70:73], v[174:177], v[226:229], v[70:73]
	v_mfma_f32_16x16x32_bf16 v[66:69], v[194:197], v[226:229], v[66:69]
	s_setprio 0
	s_barrier
	s_add_u32 s16, s50, 0x8000
	s_addc_u32 s17, s51, 0
	s_add_i32 s52, s65, s7
	s_mov_b32 m0, s52
	ds_read_b128 v[198:201], v147 offset:49152
	ds_read_b128 v[202:205], v147 offset:50176
	ds_read_b128 v[206:209], v147 offset:51200
	ds_read_b128 v[210:213], v147 offset:52224
	ds_read_b128 v[214:217], v147 offset:53248
	ds_read_b128 v[218:221], v147 offset:54272
	ds_read_b128 v[222:225], v147 offset:55296
	ds_read_b128 v[226:229], v147 offset:56320
	global_load_lds_dwordx4 v114, s[16:17]
	s_add_i32 m0, s52, 0x2000
	v_lshl_add_u64 v[144:145], s[16:17], 0, v[136:137]
	s_add_u32 s16, s50, 0x9000
	s_addc_u32 s17, s51, 0
	s_add_i32 s50, s66, s7
	global_load_lds_dwordx4 v[144:145], off
	s_mov_b32 m0, s50
	s_nop 0
	global_load_lds_dwordx4 v114, s[16:17]
	s_add_i32 m0, s50, 0x2000
	s_nop 0
	global_load_lds_dwordx4 v136, s[16:17]
	s_mov_b32 m0, s54
	s_nop 0
	global_load_lds_dwordx4 v132, s[48:49]
	s_mov_b32 m0, s55
	s_nop 0
	global_load_lds_dwordx4 v134, s[48:49]
	s_waitcnt vmcnt(8)
	s_waitcnt lgkmcnt(0)
	s_barrier
	s_setprio 1
	s_waitcnt lgkmcnt(0)
	v_mfma_f32_16x16x32_bf16 v[62:65], v[148:151], v[198:201], v[62:65]
	v_mfma_f32_16x16x32_bf16 v[58:61], v[158:161], v[198:201], v[58:61]
	v_mfma_f32_16x16x32_bf16 v[46:49], v[148:151], v[206:209], v[46:49]
	v_mfma_f32_16x16x32_bf16 v[42:45], v[158:161], v[206:209], v[42:45]
	v_mfma_f32_16x16x32_bf16 v[30:33], v[148:151], v[214:217], v[30:33]
	v_mfma_f32_16x16x32_bf16 v[26:29], v[158:161], v[214:217], v[26:29]
	v_mfma_f32_16x16x32_bf16 v[14:17], v[148:151], v[222:225], v[14:17]
	v_mfma_f32_16x16x32_bf16 v[10:13], v[158:161], v[222:225], v[10:13]
	v_mfma_f32_16x16x32_bf16 v[62:65], v[152:155], v[202:205], v[62:65]
	v_mfma_f32_16x16x32_bf16 v[58:61], v[166:169], v[202:205], v[58:61]
	v_mfma_f32_16x16x32_bf16 v[46:49], v[152:155], v[210:213], v[46:49]
	v_mfma_f32_16x16x32_bf16 v[42:45], v[166:169], v[210:213], v[42:45]
	v_mfma_f32_16x16x32_bf16 v[30:33], v[152:155], v[218:221], v[30:33]
	v_mfma_f32_16x16x32_bf16 v[26:29], v[166:169], v[218:221], v[26:29]
	v_mfma_f32_16x16x32_bf16 v[14:17], v[152:155], v[226:229], v[14:17]
	v_mfma_f32_16x16x32_bf16 v[10:13], v[166:169], v[226:229], v[10:13]
	s_setprio 0
	s_setprio 1
	v_mfma_f32_16x16x32_bf16 v[54:57], v[170:173], v[198:201], v[54:57]
	v_mfma_f32_16x16x32_bf16 v[50:53], v[178:181], v[198:201], v[50:53]
	v_mfma_f32_16x16x32_bf16 v[38:41], v[170:173], v[206:209], v[38:41]
	v_mfma_f32_16x16x32_bf16 v[34:37], v[178:181], v[206:209], v[34:37]
	v_mfma_f32_16x16x32_bf16 v[22:25], v[170:173], v[214:217], v[22:25]
	v_mfma_f32_16x16x32_bf16 v[18:21], v[178:181], v[214:217], v[18:21]
	v_mfma_f32_16x16x32_bf16 v[6:9], v[170:173], v[222:225], v[6:9]
	v_mfma_f32_16x16x32_bf16 v[2:5], v[178:181], v[222:225], v[2:5]
	v_mfma_f32_16x16x32_bf16 v[54:57], v[174:177], v[202:205], v[54:57]
	v_mfma_f32_16x16x32_bf16 v[50:53], v[194:197], v[202:205], v[50:53]
	v_mfma_f32_16x16x32_bf16 v[38:41], v[174:177], v[210:213], v[38:41]
	v_mfma_f32_16x16x32_bf16 v[34:37], v[194:197], v[210:213], v[34:37]
	v_mfma_f32_16x16x32_bf16 v[22:25], v[174:177], v[218:221], v[22:25]
	v_mfma_f32_16x16x32_bf16 v[18:21], v[194:197], v[218:221], v[18:21]
	v_mfma_f32_16x16x32_bf16 v[6:9], v[174:177], v[226:229], v[6:9]
	v_mfma_f32_16x16x32_bf16 v[2:5], v[194:197], v[226:229], v[2:5]
	s_setprio 0
	s_barrier
	s_add_i32 s64, s64, 2
	s_add_u32 s46, s46, 0x10000
	s_addc_u32 s47, s47, 0
	s_add_u32 s62, s62, 0x10000
	s_addc_u32 s63, s63, 0
	s_cmp_gt_u32 s64, 29
	s_cbranch_scc0 .LBB0_1230
	s_add_u32 s100, s60, 0xc000
	s_addc_u32 s101, s29, 0
	v_lshl_add_u64 v[144:145], s[100:101], 0, v[140:141]
	s_add_i32 m0, s20, 0xc000
	s_nop 0
	global_load_lds_dwordx4 v[144:145], off
	v_lshl_add_u64 v[144:145], s[100:101], 0, v[142:143]
	s_add_i32 m0, s20, 0xe000
	s_nop 0
	global_load_lds_dwordx4 v[144:145], off
	s_andn2_b64 vcc, s[10:11], s[38:39]
	s_cbranch_vccz .LBB0_1233
	s_barrier
.LBB0_1233:
	v_mbcnt_lo_u32_b32 v250, -1, 0
	v_mbcnt_hi_u32_b32 v250, -1, v250
	v_lshrrev_b32_e32 v251, 2, v250
	v_and_b32_e32 v250, 3, v250
	v_lshl_add_u32 v250, v250, 4, v251
	v_lshlrev_b32_e32 v250, 2, v250
	v_lshl_add_u32 v148, s59, 10, v146
	ds_read2_b32 v[150:151], v148 offset1:16
	s_lshl_b32 s17, s58, 2
	v_med3_f32 v124, v124, 0, v193
	v_med3_f32 v125, v125, 0, v193
	s_lshl_b32 s16, s44, 7
	s_or_b32 s17, s17, s45
	s_waitcnt lgkmcnt(0)
	v_mul_f32_e32 v150, v150, v150
	v_pk_mul_f32 v[124:125], v[124:125], v[124:125]
	s_add_i32 s16, s17, s16
	v_pk_mul_f32 v[152:153], v[124:125], v[150:151] op_sel_hi:[1,0]
	v_med3_f32 v124, v130, 0, v193
	v_med3_f32 v125, v131, 0, v193
	s_ashr_i32 s17, s16, 31
	v_med3_f32 v128, v128, 0, v193
	v_med3_f32 v129, v129, 0, v193
	v_med3_f32 v126, v126, 0, v193
	v_med3_f32 v127, v127, 0, v193
	v_pk_mul_f32 v[124:125], v[124:125], v[124:125]
	s_lshl_b64 s[16:17], s[16:17], 15
	v_pk_mul_f32 v[128:129], v[128:129], v[128:129]
	v_pk_mul_f32 v[130:131], v[124:125], v[150:151] op_sel_hi:[1,0]
	v_pk_mul_f32 v[124:125], v[126:127], v[126:127]
	v_med3_f32 v116, v116, 0, v193
	v_med3_f32 v117, v117, 0, v193
	v_lshl_add_u64 v[144:145], v[138:139], 0, s[16:17]
	v_pk_mul_f32 v[128:129], v[128:129], v[150:151] op_sel_hi:[1,0]
	v_pk_mul_f32 v[154:155], v[124:125], v[150:151] op_sel_hi:[1,0]
	v_cvt_pk_bf16_f32 v124, v128, v129
	v_cvt_pk_bf16_f32 v125, v130, v131
	v_pk_mul_f32 v[116:117], v[116:117], v[116:117]
	v_cvt_pk_bf16_f32 v126, v152, v153
	v_cvt_pk_bf16_f32 v127, v154, v155
	ds_bpermute_b32 v232, v250, v124
	ds_bpermute_b32 v233, v250, v125
	ds_bpermute_b32 v234, v250, v126
	ds_bpermute_b32 v235, v250, v127
	ds_bpermute_b32 v236, v250, v144
	v_med3_f32 v120, v120, 0, v193
	v_med3_f32 v121, v121, 0, v193
	v_pk_mul_f32 v[124:125], v[116:117], v[150:151] op_sel_hi:[1,0]
	v_med3_f32 v116, v122, 0, v193
	v_med3_f32 v117, v123, 0, v193
	v_med3_f32 v118, v118, 0, v193
	v_med3_f32 v119, v119, 0, v193
	v_pk_mul_f32 v[116:117], v[116:117], v[116:117]
	v_pk_mul_f32 v[120:121], v[120:121], v[120:121]
	v_pk_mul_f32 v[122:123], v[116:117], v[150:151] op_sel_hi:[1,0]
	v_pk_mul_f32 v[116:117], v[118:119], v[118:119]
	v_pk_mul_f32 v[120:121], v[120:121], v[150:151] op_sel_hi:[1,0]
	v_pk_mul_f32 v[126:127], v[116:117], v[150:151] op_sel_hi:[1,0]
	v_cvt_pk_bf16_f32 v116, v120, v121
	v_med3_f32 v106, v106, 0, v193
	v_med3_f32 v107, v107, 0, v193
	v_cvt_pk_bf16_f32 v117, v122, v123
	v_cvt_pk_bf16_f32 v118, v124, v125
	v_cvt_pk_bf16_f32 v119, v126, v127
	ds_bpermute_b32 v238, v250, v116
	ds_bpermute_b32 v239, v250, v117
	ds_bpermute_b32 v240, v250, v118
	ds_bpermute_b32 v241, v250, v119
	ds_bpermute_b32 v242, v250, v144
	v_pk_mul_f32 v[106:107], v[106:107], v[106:107]
	v_med3_f32 v110, v110, 0, v193
	v_mul_f32_e32 v116, v151, v151
	v_pk_mul_f32 v[118:119], v[106:107], v[116:117] op_sel_hi:[1,0]
	v_med3_f32 v106, v112, 0, v193
	v_med3_f32 v107, v113, 0, v193
	v_med3_f32 v111, v111, 0, v193
	v_med3_f32 v108, v108, 0, v193
	v_med3_f32 v109, v109, 0, v193
	v_pk_mul_f32 v[106:107], v[106:107], v[106:107]
	v_pk_mul_f32 v[110:111], v[110:111], v[110:111]
	v_pk_mul_f32 v[112:113], v[106:107], v[116:117] op_sel_hi:[1,0]
	v_pk_mul_f32 v[106:107], v[108:109], v[108:109]
	v_med3_f32 v98, v98, 0, v193
	v_med3_f32 v99, v99, 0, v193
	v_pk_mul_f32 v[110:111], v[110:111], v[116:117] op_sel_hi:[1,0]
	v_pk_mul_f32 v[120:121], v[106:107], v[116:117] op_sel_hi:[1,0]
	v_cvt_pk_bf16_f32 v106, v110, v111
	v_cvt_pk_bf16_f32 v107, v112, v113
	v_pk_mul_f32 v[98:99], v[98:99], v[98:99]
	v_cvt_pk_bf16_f32 v108, v118, v119
	v_cvt_pk_bf16_f32 v109, v120, v121
	s_waitcnt lgkmcnt(5)
	v_subrev_u32_e32 v236, s82, v236
	global_store_dwordx4 v236, v[232:235], s[82:83]
	ds_bpermute_b32 v244, v250, v106
	ds_bpermute_b32 v245, v250, v107
	ds_bpermute_b32 v246, v250, v108
	ds_bpermute_b32 v247, v250, v109
	ds_bpermute_b32 v248, v250, v144
	v_med3_f32 v102, v102, 0, v193
	v_med3_f32 v103, v103, 0, v193
	v_pk_mul_f32 v[106:107], v[98:99], v[116:117] op_sel_hi:[1,0]
	v_med3_f32 v98, v104, 0, v193
	v_med3_f32 v99, v105, 0, v193
	v_pk_mul_f32 v[102:103], v[102:103], v[102:103]
	v_med3_f32 v100, v100, 0, v193
	v_med3_f32 v101, v101, 0, v193
	v_pk_mul_f32 v[98:99], v[98:99], v[98:99]
	v_pk_mul_f32 v[102:103], v[102:103], v[116:117] op_sel_hi:[1,0]
	v_pk_mul_f32 v[104:105], v[98:99], v[116:117] op_sel_hi:[1,0]
	v_pk_mul_f32 v[98:99], v[100:101], v[100:101]
	v_med3_f32 v90, v90, 0, v193
	v_pk_mul_f32 v[108:109], v[98:99], v[116:117] op_sel_hi:[1,0]
	v_cvt_pk_bf16_f32 v98, v102, v103
	ds_read2_b32 v[102:103], v148 offset0:32 offset1:48
	v_med3_f32 v91, v91, 0, v193
	v_cvt_pk_bf16_f32 v99, v104, v105
	v_cvt_pk_bf16_f32 v100, v106, v107
	v_cvt_pk_bf16_f32 v101, v108, v109
	s_waitcnt lgkmcnt(6)
	v_subrev_u32_e32 v242, s82, v242
	global_store_dwordx4 v242, v[238:241], s[82:83] offset:64
	ds_bpermute_b32 v232, v250, v98
	ds_bpermute_b32 v233, v250, v99
	ds_bpermute_b32 v234, v250, v100
	ds_bpermute_b32 v235, v250, v101
	ds_bpermute_b32 v236, v250, v144
	v_pk_mul_f32 v[90:91], v[90:91], v[90:91]
	v_med3_f32 v94, v94, 0, v193
	s_waitcnt lgkmcnt(0)
	v_mul_f32_e32 v98, v102, v102
	v_med3_f32 v95, v95, 0, v193
	v_pk_mul_f32 v[100:101], v[90:91], v[98:99] op_sel_hi:[1,0]
	v_med3_f32 v90, v96, 0, v193
	v_med3_f32 v91, v97, 0, v193
	v_pk_mul_f32 v[94:95], v[94:95], v[94:95]
	v_med3_f32 v92, v92, 0, v193
	v_med3_f32 v93, v93, 0, v193
	v_pk_mul_f32 v[90:91], v[90:91], v[90:91]
	v_pk_mul_f32 v[94:95], v[94:95], v[98:99] op_sel_hi:[1,0]
	v_pk_mul_f32 v[96:97], v[90:91], v[98:99] op_sel_hi:[1,0]
	v_pk_mul_f32 v[90:91], v[92:93], v[92:93]
	v_med3_f32 v82, v82, 0, v193
	v_pk_mul_f32 v[104:105], v[90:91], v[98:99] op_sel_hi:[1,0]
	v_cvt_pk_bf16_f32 v90, v94, v95
	v_add_co_u32_e32 v94, vcc, s73, v144
	v_med3_f32 v83, v83, 0, v193
	v_cvt_pk_bf16_f32 v91, v96, v97
	s_nop 0
	v_addc_co_u32_e32 v95, vcc, 0, v145, vcc
	v_pk_mul_f32 v[82:83], v[82:83], v[82:83]
	v_cvt_pk_bf16_f32 v92, v100, v101
	v_cvt_pk_bf16_f32 v93, v104, v105
	s_waitcnt lgkmcnt(6)
	v_subrev_u32_e32 v248, s82, v248
	global_store_dwordx4 v248, v[244:247], s[82:83] offset:2048
	ds_bpermute_b32 v238, v250, v90
	ds_bpermute_b32 v239, v250, v91
	ds_bpermute_b32 v240, v250, v92
	ds_bpermute_b32 v241, v250, v93
	ds_bpermute_b32 v242, v250, v94
	v_med3_f32 v86, v86, 0, v193
	v_med3_f32 v87, v87, 0, v193
	v_pk_mul_f32 v[90:91], v[82:83], v[98:99] op_sel_hi:[1,0]
	v_med3_f32 v82, v88, 0, v193
	v_med3_f32 v83, v89, 0, v193
	v_med3_f32 v84, v84, 0, v193
	v_med3_f32 v85, v85, 0, v193
	v_pk_mul_f32 v[82:83], v[82:83], v[82:83]
	v_pk_mul_f32 v[86:87], v[86:87], v[86:87]
	v_pk_mul_f32 v[88:89], v[82:83], v[98:99] op_sel_hi:[1,0]
	v_pk_mul_f32 v[82:83], v[84:85], v[84:85]
	v_pk_mul_f32 v[86:87], v[86:87], v[98:99] op_sel_hi:[1,0]
	v_pk_mul_f32 v[92:93], v[82:83], v[98:99] op_sel_hi:[1,0]
	v_cvt_pk_bf16_f32 v82, v86, v87
	v_med3_f32 v74, v74, 0, v193
	v_med3_f32 v75, v75, 0, v193
	v_cvt_pk_bf16_f32 v83, v88, v89
	v_cvt_pk_bf16_f32 v84, v90, v91
	v_cvt_pk_bf16_f32 v85, v92, v93
	s_waitcnt lgkmcnt(5)
	v_subrev_u32_e32 v236, s82, v236
	global_store_dwordx4 v236, v[232:235], s[82:83] offset:2112
	ds_bpermute_b32 v244, v250, v82
	ds_bpermute_b32 v245, v250, v83
	ds_bpermute_b32 v246, v250, v84
	ds_bpermute_b32 v247, v250, v85
	ds_bpermute_b32 v248, v250, v94
	v_pk_mul_f32 v[74:75], v[74:75], v[74:75]
	v_med3_f32 v78, v78, 0, v193
	v_mul_f32_e32 v82, v103, v103
	v_pk_mul_f32 v[84:85], v[74:75], v[82:83] op_sel_hi:[1,0]
	v_med3_f32 v74, v80, 0, v193
	v_med3_f32 v75, v81, 0, v193
	v_med3_f32 v79, v79, 0, v193
	v_med3_f32 v76, v76, 0, v193
	v_med3_f32 v77, v77, 0, v193
	v_pk_mul_f32 v[74:75], v[74:75], v[74:75]
	v_pk_mul_f32 v[78:79], v[78:79], v[78:79]
	v_pk_mul_f32 v[80:81], v[74:75], v[82:83] op_sel_hi:[1,0]
	v_pk_mul_f32 v[74:75], v[76:77], v[76:77]
	v_med3_f32 v66, v66, 0, v193
	v_med3_f32 v67, v67, 0, v193
	v_pk_mul_f32 v[78:79], v[78:79], v[82:83] op_sel_hi:[1,0]
	v_pk_mul_f32 v[86:87], v[74:75], v[82:83] op_sel_hi:[1,0]
	v_cvt_pk_bf16_f32 v74, v78, v79
	v_cvt_pk_bf16_f32 v75, v80, v81
	v_pk_mul_f32 v[66:67], v[66:67], v[66:67]
	v_cvt_pk_bf16_f32 v76, v84, v85
	v_cvt_pk_bf16_f32 v77, v86, v87
	s_waitcnt lgkmcnt(5)
	v_subrev_u32_e32 v242, s82, v242
	global_store_dwordx4 v242, v[238:241], s[82:83]
	ds_bpermute_b32 v232, v250, v74
	ds_bpermute_b32 v233, v250, v75
	ds_bpermute_b32 v234, v250, v76
	ds_bpermute_b32 v235, v250, v77
	ds_bpermute_b32 v236, v250, v94
	v_med3_f32 v70, v70, 0, v193
	v_med3_f32 v71, v71, 0, v193
	v_pk_mul_f32 v[74:75], v[66:67], v[82:83] op_sel_hi:[1,0]
	v_med3_f32 v66, v72, 0, v193
	v_med3_f32 v67, v73, 0, v193
	v_pk_mul_f32 v[70:71], v[70:71], v[70:71]
	v_med3_f32 v68, v68, 0, v193
	v_med3_f32 v69, v69, 0, v193
	v_pk_mul_f32 v[66:67], v[66:67], v[66:67]
	v_pk_mul_f32 v[70:71], v[70:71], v[82:83] op_sel_hi:[1,0]
	v_pk_mul_f32 v[72:73], v[66:67], v[82:83] op_sel_hi:[1,0]
	v_pk_mul_f32 v[66:67], v[68:69], v[68:69]
	v_med3_f32 v64, v64, 0, v193
	v_pk_mul_f32 v[76:77], v[66:67], v[82:83] op_sel_hi:[1,0]
	v_cvt_pk_bf16_f32 v66, v70, v71
	ds_read2_b32 v[70:71], v148 offset0:128 offset1:144
	v_med3_f32 v65, v65, 0, v193
	v_cvt_pk_bf16_f32 v67, v72, v73
	v_cvt_pk_bf16_f32 v68, v74, v75
	v_cvt_pk_bf16_f32 v69, v76, v77
	s_waitcnt lgkmcnt(6)
	v_subrev_u32_e32 v248, s82, v248
	global_store_dwordx4 v248, v[244:247], s[82:83] offset:64
	ds_bpermute_b32 v238, v250, v66
	ds_bpermute_b32 v239, v250, v67
	ds_bpermute_b32 v240, v250, v68
	ds_bpermute_b32 v241, v250, v69
	ds_bpermute_b32 v242, v250, v94
	v_med3_f32 v60, v60, 0, v193
	v_med3_f32 v61, v61, 0, v193
	s_waitcnt lgkmcnt(0)
	v_mul_f32_e32 v66, v70, v70
	v_pk_mul_f32 v[64:65], v[64:65], v[64:65]
	v_med3_f32 v62, v62, 0, v193
	v_med3_f32 v63, v63, 0, v193
	v_med3_f32 v58, v58, 0, v193
	v_med3_f32 v59, v59, 0, v193
	v_pk_mul_f32 v[64:65], v[64:65], v[66:67] op_sel_hi:[1,0]
	v_pk_mul_f32 v[60:61], v[60:61], v[60:61]
	v_pk_mul_f32 v[62:63], v[62:63], v[62:63]
	v_pk_mul_f32 v[58:59], v[58:59], v[58:59]
	v_pk_mul_f32 v[68:69], v[60:61], v[66:67] op_sel_hi:[1,0]
	v_cvt_pk_bf16_f32 v61, v64, v65
	v_add_co_u32_e32 v64, vcc, s72, v144
	v_pk_mul_f32 v[62:63], v[62:63], v[66:67] op_sel_hi:[1,0]
	v_pk_mul_f32 v[58:59], v[58:59], v[66:67] op_sel_hi:[1,0]
	v_addc_co_u32_e32 v65, vcc, 0, v145, vcc
	v_cvt_pk_bf16_f32 v60, v62, v63
	v_cvt_pk_bf16_f32 v62, v58, v59
	v_add_co_u32_e32 v58, vcc, s31, v144
	v_med3_f32 v50, v50, 0, v193
	v_med3_f32 v51, v51, 0, v193
	v_addc_co_u32_e32 v59, vcc, 0, v145, vcc
	v_pk_mul_f32 v[50:51], v[50:51], v[50:51]
	v_cvt_pk_bf16_f32 v63, v68, v69
	s_waitcnt lgkmcnt(6)
	v_subrev_u32_e32 v236, s82, v236
	global_store_dwordx4 v236, v[232:235], s[82:83] offset:2048
	ds_bpermute_b32 v244, v250, v60
	ds_bpermute_b32 v245, v250, v61
	ds_bpermute_b32 v246, v250, v62
	ds_bpermute_b32 v247, v250, v63
	ds_bpermute_b32 v248, v250, v58
	v_med3_f32 v54, v54, 0, v193
	v_med3_f32 v55, v55, 0, v193
	v_pk_mul_f32 v[60:61], v[50:51], v[66:67] op_sel_hi:[1,0]
	v_med3_f32 v50, v56, 0, v193
	v_med3_f32 v51, v57, 0, v193
	v_med3_f32 v52, v52, 0, v193
	v_med3_f32 v53, v53, 0, v193
	v_pk_mul_f32 v[50:51], v[50:51], v[50:51]
	v_pk_mul_f32 v[54:55], v[54:55], v[54:55]
	v_pk_mul_f32 v[56:57], v[50:51], v[66:67] op_sel_hi:[1,0]
	v_pk_mul_f32 v[50:51], v[52:53], v[52:53]
	v_pk_mul_f32 v[54:55], v[54:55], v[66:67] op_sel_hi:[1,0]
	v_pk_mul_f32 v[62:63], v[50:51], v[66:67] op_sel_hi:[1,0]
	v_cvt_pk_bf16_f32 v50, v54, v55
	v_med3_f32 v42, v42, 0, v193
	v_med3_f32 v43, v43, 0, v193
	v_cvt_pk_bf16_f32 v51, v56, v57
	v_cvt_pk_bf16_f32 v52, v60, v61
	v_cvt_pk_bf16_f32 v53, v62, v63
	s_waitcnt lgkmcnt(5)
	v_subrev_u32_e32 v242, s82, v242
	global_store_dwordx4 v242, v[238:241], s[82:83] offset:2112
	ds_bpermute_b32 v232, v250, v50
	ds_bpermute_b32 v233, v250, v51
	ds_bpermute_b32 v234, v250, v52
	ds_bpermute_b32 v235, v250, v53
	ds_bpermute_b32 v236, v250, v64
	v_pk_mul_f32 v[42:43], v[42:43], v[42:43]
	v_med3_f32 v46, v46, 0, v193
	v_mul_f32_e32 v50, v71, v71
	v_pk_mul_f32 v[52:53], v[42:43], v[50:51] op_sel_hi:[1,0]
	v_med3_f32 v42, v48, 0, v193
	v_med3_f32 v43, v49, 0, v193
	v_med3_f32 v47, v47, 0, v193
	v_med3_f32 v44, v44, 0, v193
	v_med3_f32 v45, v45, 0, v193
	v_pk_mul_f32 v[42:43], v[42:43], v[42:43]
	v_pk_mul_f32 v[46:47], v[46:47], v[46:47]
	v_pk_mul_f32 v[48:49], v[42:43], v[50:51] op_sel_hi:[1,0]
	v_pk_mul_f32 v[42:43], v[44:45], v[44:45]
	v_med3_f32 v34, v34, 0, v193
	v_med3_f32 v35, v35, 0, v193
	v_pk_mul_f32 v[46:47], v[46:47], v[50:51] op_sel_hi:[1,0]
	v_pk_mul_f32 v[54:55], v[42:43], v[50:51] op_sel_hi:[1,0]
	v_cvt_pk_bf16_f32 v42, v46, v47
	v_cvt_pk_bf16_f32 v43, v48, v49
	v_pk_mul_f32 v[34:35], v[34:35], v[34:35]
	v_cvt_pk_bf16_f32 v44, v52, v53
	v_cvt_pk_bf16_f32 v45, v54, v55
	s_waitcnt lgkmcnt(5)
	v_subrev_u32_e32 v248, s82, v248
	global_store_dwordx4 v248, v[244:247], s[82:83] offset:-4096
	ds_bpermute_b32 v238, v250, v42
	ds_bpermute_b32 v239, v250, v43
	ds_bpermute_b32 v240, v250, v44
	ds_bpermute_b32 v241, v250, v45
	ds_bpermute_b32 v242, v250, v64
	v_med3_f32 v38, v38, 0, v193
	v_med3_f32 v39, v39, 0, v193
	v_pk_mul_f32 v[42:43], v[34:35], v[50:51] op_sel_hi:[1,0]
	v_med3_f32 v34, v40, 0, v193
	v_med3_f32 v35, v41, 0, v193
	v_pk_mul_f32 v[38:39], v[38:39], v[38:39]
	v_med3_f32 v36, v36, 0, v193
	v_med3_f32 v37, v37, 0, v193
	v_pk_mul_f32 v[34:35], v[34:35], v[34:35]
	v_pk_mul_f32 v[38:39], v[38:39], v[50:51] op_sel_hi:[1,0]
	v_pk_mul_f32 v[40:41], v[34:35], v[50:51] op_sel_hi:[1,0]
	v_pk_mul_f32 v[34:35], v[36:37], v[36:37]
	v_med3_f32 v26, v26, 0, v193
	v_pk_mul_f32 v[44:45], v[34:35], v[50:51] op_sel_hi:[1,0]
	v_cvt_pk_bf16_f32 v34, v38, v39
	ds_read2_b32 v[38:39], v148 offset0:160 offset1:176
	v_med3_f32 v27, v27, 0, v193
	v_cvt_pk_bf16_f32 v35, v40, v41
	v_cvt_pk_bf16_f32 v36, v42, v43
	v_cvt_pk_bf16_f32 v37, v44, v45
	s_waitcnt lgkmcnt(6)
	v_subrev_u32_e32 v236, s82, v236
	global_store_dwordx4 v236, v[232:235], s[82:83] offset:64
	ds_bpermute_b32 v244, v250, v34
	ds_bpermute_b32 v245, v250, v35
	ds_bpermute_b32 v246, v250, v36
	ds_bpermute_b32 v247, v250, v37
	ds_bpermute_b32 v248, v250, v64
	v_pk_mul_f32 v[26:27], v[26:27], v[26:27]
	v_med3_f32 v30, v30, 0, v193
	s_waitcnt lgkmcnt(0)
	v_mul_f32_e32 v34, v38, v38
	v_pk_mul_f32 v[36:37], v[26:27], v[34:35] op_sel_hi:[1,0]
	v_med3_f32 v26, v32, 0, v193
	v_med3_f32 v27, v33, 0, v193
	v_med3_f32 v31, v31, 0, v193
	v_med3_f32 v28, v28, 0, v193
	v_med3_f32 v29, v29, 0, v193
	v_pk_mul_f32 v[26:27], v[26:27], v[26:27]
	v_pk_mul_f32 v[30:31], v[30:31], v[30:31]
	v_pk_mul_f32 v[32:33], v[26:27], v[34:35] op_sel_hi:[1,0]
	v_pk_mul_f32 v[26:27], v[28:29], v[28:29]
	v_med3_f32 v18, v18, 0, v193
	v_med3_f32 v19, v19, 0, v193
	v_pk_mul_f32 v[30:31], v[30:31], v[34:35] op_sel_hi:[1,0]
	v_pk_mul_f32 v[40:41], v[26:27], v[34:35] op_sel_hi:[1,0]
	v_cvt_pk_bf16_f32 v26, v30, v31
	v_cvt_pk_bf16_f32 v27, v32, v33
	v_pk_mul_f32 v[18:19], v[18:19], v[18:19]
	v_cvt_pk_bf16_f32 v28, v36, v37
	v_cvt_pk_bf16_f32 v29, v40, v41
	s_waitcnt lgkmcnt(6)
	v_subrev_u32_e32 v242, s82, v242
	global_store_dwordx4 v242, v[238:241], s[82:83] offset:2048
	ds_bpermute_b32 v232, v250, v26
	ds_bpermute_b32 v233, v250, v27
	ds_bpermute_b32 v234, v250, v28
	ds_bpermute_b32 v235, v250, v29
	ds_bpermute_b32 v236, v250, v58
	v_med3_f32 v22, v22, 0, v193
	v_med3_f32 v23, v23, 0, v193
	v_pk_mul_f32 v[26:27], v[18:19], v[34:35] op_sel_hi:[1,0]
	v_med3_f32 v18, v24, 0, v193
	v_med3_f32 v19, v25, 0, v193
	v_med3_f32 v20, v20, 0, v193
	v_med3_f32 v21, v21, 0, v193
	v_pk_mul_f32 v[18:19], v[18:19], v[18:19]
	v_pk_mul_f32 v[22:23], v[22:23], v[22:23]
	v_pk_mul_f32 v[24:25], v[18:19], v[34:35] op_sel_hi:[1,0]
	v_pk_mul_f32 v[18:19], v[20:21], v[20:21]
	v_pk_mul_f32 v[22:23], v[22:23], v[34:35] op_sel_hi:[1,0]
	v_pk_mul_f32 v[28:29], v[18:19], v[34:35] op_sel_hi:[1,0]
	v_cvt_pk_bf16_f32 v18, v22, v23
	v_med3_f32 v10, v10, 0, v193
	v_med3_f32 v11, v11, 0, v193
	v_cvt_pk_bf16_f32 v19, v24, v25
	v_cvt_pk_bf16_f32 v20, v26, v27
	v_cvt_pk_bf16_f32 v21, v28, v29
	s_waitcnt lgkmcnt(5)
	v_subrev_u32_e32 v248, s82, v248
	global_store_dwordx4 v248, v[244:247], s[82:83] offset:2112
	ds_bpermute_b32 v238, v250, v18
	ds_bpermute_b32 v239, v250, v19
	ds_bpermute_b32 v240, v250, v20
	ds_bpermute_b32 v241, v250, v21
	ds_bpermute_b32 v242, v250, v58
	v_pk_mul_f32 v[10:11], v[10:11], v[10:11]
	v_med3_f32 v14, v14, 0, v193
	v_mul_f32_e32 v18, v39, v39
	v_pk_mul_f32 v[20:21], v[10:11], v[18:19] op_sel_hi:[1,0]
	v_med3_f32 v10, v16, 0, v193
	v_med3_f32 v11, v17, 0, v193
	v_med3_f32 v15, v15, 0, v193
	v_med3_f32 v12, v12, 0, v193
	v_med3_f32 v13, v13, 0, v193
	v_pk_mul_f32 v[10:11], v[10:11], v[10:11]
	v_pk_mul_f32 v[14:15], v[14:15], v[14:15]
	v_pk_mul_f32 v[16:17], v[10:11], v[18:19] op_sel_hi:[1,0]
	v_pk_mul_f32 v[10:11], v[12:13], v[12:13]
	v_med3_f32 v2, v2, 0, v193
	v_med3_f32 v3, v3, 0, v193
	v_pk_mul_f32 v[14:15], v[14:15], v[18:19] op_sel_hi:[1,0]
	v_pk_mul_f32 v[22:23], v[10:11], v[18:19] op_sel_hi:[1,0]
	v_cvt_pk_bf16_f32 v10, v14, v15
	v_cvt_pk_bf16_f32 v11, v16, v17
	v_pk_mul_f32 v[2:3], v[2:3], v[2:3]
	v_cvt_pk_bf16_f32 v12, v20, v21
	v_cvt_pk_bf16_f32 v13, v22, v23
	s_waitcnt lgkmcnt(5)
	v_subrev_u32_e32 v236, s82, v236
	global_store_dwordx4 v236, v[232:235], s[82:83]
	ds_bpermute_b32 v244, v250, v10
	ds_bpermute_b32 v245, v250, v11
	ds_bpermute_b32 v246, v250, v12
	ds_bpermute_b32 v247, v250, v13
	ds_bpermute_b32 v248, v250, v58
	v_med3_f32 v6, v6, 0, v193
	v_med3_f32 v7, v7, 0, v193
	v_pk_mul_f32 v[10:11], v[2:3], v[18:19] op_sel_hi:[1,0]
	v_med3_f32 v2, v8, 0, v193
	v_med3_f32 v3, v9, 0, v193
	v_med3_f32 v4, v4, 0, v193
	v_med3_f32 v5, v5, 0, v193
	v_pk_mul_f32 v[2:3], v[2:3], v[2:3]
	v_pk_mul_f32 v[6:7], v[6:7], v[6:7]
	v_pk_mul_f32 v[8:9], v[2:3], v[18:19] op_sel_hi:[1,0]
	v_pk_mul_f32 v[2:3], v[4:5], v[4:5]
	s_andn2_b64 vcc, exec, s[38:39]
	s_mov_b64 s[38:39], -1
	v_pk_mul_f32 v[6:7], v[6:7], v[18:19] op_sel_hi:[1,0]
	v_pk_mul_f32 v[12:13], v[2:3], v[18:19] op_sel_hi:[1,0]
	v_cvt_pk_bf16_f32 v2, v6, v7
	v_cvt_pk_bf16_f32 v3, v8, v9
	v_cvt_pk_bf16_f32 v4, v10, v11
	s_nop 0
	v_cvt_pk_bf16_f32 v5, v12, v13
	s_waitcnt lgkmcnt(5)
	v_subrev_u32_e32 v242, s82, v242
	global_store_dwordx4 v242, v[238:241], s[82:83] offset:64
	ds_bpermute_b32 v232, v250, v2
	ds_bpermute_b32 v233, v250, v3
	ds_bpermute_b32 v234, v250, v4
	ds_bpermute_b32 v235, v250, v5
	ds_bpermute_b32 v236, v250, v58
	s_waitcnt lgkmcnt(5)
	v_subrev_u32_e32 v248, s82, v248
	global_store_dwordx4 v248, v[244:247], s[82:83] offset:2048
	s_waitcnt lgkmcnt(0)
	v_subrev_u32_e32 v236, s82, v236
	global_store_dwordx4 v236, v[232:235], s[82:83] offset:2112
	s_cbranch_vccnz .LBB0_1222
	s_andn2_b64 vcc, exec, s[0:1]
	s_cbranch_vccnz .LBB0_1221
	s_branch .LBB0_1221
